# speedup vs baseline: 1.0212x; 1.0212x over previous
_Z12final_kernelPKDF16_S0_PKfS2_S2_S2_Pf:
	s_load_dwordx8 s[4:11], s[0:1], 0x0
	s_load_dwordx2 s[14:15], s[0:1], 0x20
	s_load_dwordx4 s[16:19], s[0:1], 0x28
	v_readfirstlane_b32 s3, v0
	v_bfe_u32 v70, v0, 4, 2
	v_and_b32_e32 v71, 15, v0
	s_lshr_b32 s3, s3, 6
	s_lshl_b32 s12, s2, 4
	s_lshl_b32 s20, s2, 11
	s_lshl_b32 s21, s3, 7
	s_lshl_b32 s22, s3, 6
	v_lshlrev_b32_e32 v72, 7, v71
	v_lshl_or_b32 v72, v70, 5, v72
	v_lshlrev_b32_e32 v73, 12, v70
	v_lshl_or_b32 v73, v71, 2, v73
	v_lshlrev_b32_e32 v74, 2, v71
	v_lshlrev_b32_e32 v75, 9, v70
	v_lshl_or_b32 v75, v71, 1, v75
	s_add_i32 s23, s22, 0x1080
	v_lshl_add_u32 v76, v70, 4, s23
	s_waitcnt lgkmcnt(0)
	s_load_dword s13, s[16:17], 0x0
	s_add_u32 s4, s4, s20
	s_addc_u32 s5, s5, 0
	s_add_u32 s8, s8, s21
	s_addc_u32 s9, s9, 0
	global_load_dwordx4 v[2:5], v72, s[4:5] nt
	global_load_dwordx4 v[6:9], v72, s[4:5] offset:16 nt
	global_load_dword v26, v73, s[8:9]
	global_load_dword v42, v73, s[8:9] offset:64
	global_load_dword v27, v73, s[8:9] offset:256
	global_load_dword v43, v73, s[8:9] offset:320
	global_load_dword v28, v73, s[8:9] offset:512
	global_load_dword v44, v73, s[8:9] offset:576
	global_load_dword v29, v73, s[8:9] offset:768
	global_load_dword v45, v73, s[8:9] offset:832
	global_load_dword v30, v73, s[8:9] offset:1024
	global_load_dword v46, v73, s[8:9] offset:1088
	global_load_dword v31, v73, s[8:9] offset:1280
	global_load_dword v47, v73, s[8:9] offset:1344
	global_load_dword v32, v73, s[8:9] offset:1536
	global_load_dword v48, v73, s[8:9] offset:1600
	global_load_dword v33, v73, s[8:9] offset:1792
	global_load_dword v49, v73, s[8:9] offset:1856
	global_load_dword v34, v73, s[8:9] offset:2048
	global_load_dword v50, v73, s[8:9] offset:2112
	global_load_dword v35, v73, s[8:9] offset:2304
	global_load_dword v51, v73, s[8:9] offset:2368
	global_load_dword v36, v73, s[8:9] offset:2560
	global_load_dword v52, v73, s[8:9] offset:2624
	global_load_dword v37, v73, s[8:9] offset:2816
	global_load_dword v53, v73, s[8:9] offset:2880
	global_load_dword v38, v73, s[8:9] offset:3072
	global_load_dword v54, v73, s[8:9] offset:3136
	global_load_dword v39, v73, s[8:9] offset:3328
	global_load_dword v55, v73, s[8:9] offset:3392
	global_load_dword v40, v73, s[8:9] offset:3584
	global_load_dword v56, v73, s[8:9] offset:3648
	global_load_dword v41, v73, s[8:9] offset:3840
	global_load_dword v57, v73, s[8:9] offset:3904
	s_add_u32 s6, s6, s20
	s_addc_u32 s7, s7, 0
	s_add_u32 s6, s6, s22
	s_addc_u32 s7, s7, 0
	global_load_ushort v60, v75, s[6:7] nt
	global_load_ushort v64, v75, s[6:7] offset:32 nt
	global_load_ushort v61, v75, s[6:7] offset:128 nt
	global_load_ushort v65, v75, s[6:7] offset:160 nt
	global_load_ushort v62, v75, s[6:7] offset:256 nt
	global_load_ushort v66, v75, s[6:7] offset:288 nt
	global_load_ushort v63, v75, s[6:7] offset:384 nt
	global_load_ushort v67, v75, s[6:7] offset:416 nt
	s_add_u32 s10, s10, s21
	s_addc_u32 s11, s11, 0
	global_load_dword v58, v74, s[10:11]
	global_load_dword v59, v74, s[10:11] offset:64
	s_add_u32 s14, s14, s21
	s_addc_u32 s15, s15, 0
	global_load_dword v68, v74, s[14:15]
	global_load_dword v69, v74, s[14:15] offset:64
	v_accvgpr_write_b32 a0, 0
	v_accvgpr_write_b32 a1, 0
	v_accvgpr_write_b32 a2, 0
	v_accvgpr_write_b32 a3, 0
	v_accvgpr_write_b32 a4, 0
	v_accvgpr_write_b32 a5, 0
	v_accvgpr_write_b32 a6, 0
	v_accvgpr_write_b32 a7, 0
	s_waitcnt vmcnt(44)
	v_cvt_f32_f16_e32 v10, v2
	v_cvt_f32_f16_sdwa v11, v2 dst_sel:DWORD dst_unused:UNUSED_PAD src0_sel:WORD_1
	v_cvt_f32_f16_e32 v12, v3
	v_cvt_f32_f16_sdwa v13, v3 dst_sel:DWORD dst_unused:UNUSED_PAD src0_sel:WORD_1
	v_cvt_f32_f16_e32 v14, v4
	v_cvt_f32_f16_sdwa v15, v4 dst_sel:DWORD dst_unused:UNUSED_PAD src0_sel:WORD_1
	v_cvt_f32_f16_e32 v16, v5
	v_cvt_f32_f16_sdwa v17, v5 dst_sel:DWORD dst_unused:UNUSED_PAD src0_sel:WORD_1
	v_cvt_f32_f16_e32 v18, v6
	v_cvt_f32_f16_sdwa v19, v6 dst_sel:DWORD dst_unused:UNUSED_PAD src0_sel:WORD_1
	v_cvt_f32_f16_e32 v20, v7
	v_cvt_f32_f16_sdwa v21, v7 dst_sel:DWORD dst_unused:UNUSED_PAD src0_sel:WORD_1
	v_cvt_f32_f16_e32 v22, v8
	v_cvt_f32_f16_sdwa v23, v8 dst_sel:DWORD dst_unused:UNUSED_PAD src0_sel:WORD_1
	v_cvt_f32_f16_e32 v24, v9
	v_cvt_f32_f16_sdwa v25, v9 dst_sel:DWORD dst_unused:UNUSED_PAD src0_sel:WORD_1
	v_max_f32_e32 v10, 0, v10
	v_max_f32_e32 v11, 0, v11
	v_max_f32_e32 v12, 0, v12
	v_max_f32_e32 v13, 0, v13
	v_max_f32_e32 v14, 0, v14
	v_max_f32_e32 v15, 0, v15
	v_max_f32_e32 v16, 0, v16
	v_max_f32_e32 v17, 0, v17
	v_max_f32_e32 v18, 0, v18
	v_max_f32_e32 v19, 0, v19
	v_max_f32_e32 v20, 0, v20
	v_max_f32_e32 v21, 0, v21
	v_max_f32_e32 v22, 0, v22
	v_max_f32_e32 v23, 0, v23
	v_max_f32_e32 v24, 0, v24
	v_max_f32_e32 v25, 0, v25
	s_waitcnt vmcnt(42)
	v_mfma_f32_16x16x4_f32 a[0:3], v10, v26, a[0:3]
	v_mfma_f32_16x16x4_f32 a[4:7], v10, v42, a[4:7]
	s_waitcnt vmcnt(40)
	v_mfma_f32_16x16x4_f32 a[0:3], v11, v27, a[0:3]
	v_mfma_f32_16x16x4_f32 a[4:7], v11, v43, a[4:7]
	s_waitcnt vmcnt(38)
	v_mfma_f32_16x16x4_f32 a[0:3], v12, v28, a[0:3]
	v_mfma_f32_16x16x4_f32 a[4:7], v12, v44, a[4:7]
	s_waitcnt vmcnt(36)
	v_mfma_f32_16x16x4_f32 a[0:3], v13, v29, a[0:3]
	v_mfma_f32_16x16x4_f32 a[4:7], v13, v45, a[4:7]
	s_waitcnt vmcnt(34)
	v_mfma_f32_16x16x4_f32 a[0:3], v14, v30, a[0:3]
	v_mfma_f32_16x16x4_f32 a[4:7], v14, v46, a[4:7]
	s_waitcnt vmcnt(32)
	v_mfma_f32_16x16x4_f32 a[0:3], v15, v31, a[0:3]
	v_mfma_f32_16x16x4_f32 a[4:7], v15, v47, a[4:7]
	s_waitcnt vmcnt(30)
	v_mfma_f32_16x16x4_f32 a[0:3], v16, v32, a[0:3]
	v_mfma_f32_16x16x4_f32 a[4:7], v16, v48, a[4:7]
	s_waitcnt vmcnt(28)
	v_mfma_f32_16x16x4_f32 a[0:3], v17, v33, a[0:3]
	v_mfma_f32_16x16x4_f32 a[4:7], v17, v49, a[4:7]
	s_waitcnt vmcnt(26)
	v_mfma_f32_16x16x4_f32 a[0:3], v18, v34, a[0:3]
	v_mfma_f32_16x16x4_f32 a[4:7], v18, v50, a[4:7]
	s_waitcnt vmcnt(24)
	v_mfma_f32_16x16x4_f32 a[0:3], v19, v35, a[0:3]
	v_mfma_f32_16x16x4_f32 a[4:7], v19, v51, a[4:7]
	s_waitcnt vmcnt(22)
	v_mfma_f32_16x16x4_f32 a[0:3], v20, v36, a[0:3]
	v_mfma_f32_16x16x4_f32 a[4:7], v20, v52, a[4:7]
	s_waitcnt vmcnt(20)
	v_mfma_f32_16x16x4_f32 a[0:3], v21, v37, a[0:3]
	v_mfma_f32_16x16x4_f32 a[4:7], v21, v53, a[4:7]
	s_waitcnt vmcnt(18)
	v_mfma_f32_16x16x4_f32 a[0:3], v22, v38, a[0:3]
	v_mfma_f32_16x16x4_f32 a[4:7], v22, v54, a[4:7]
	s_waitcnt vmcnt(16)
	v_mfma_f32_16x16x4_f32 a[0:3], v23, v39, a[0:3]
	v_mfma_f32_16x16x4_f32 a[4:7], v23, v55, a[4:7]
	s_waitcnt vmcnt(14)
	v_mfma_f32_16x16x4_f32 a[0:3], v24, v40, a[0:3]
	v_mfma_f32_16x16x4_f32 a[4:7], v24, v56, a[4:7]
	s_waitcnt vmcnt(12)
	v_mfma_f32_16x16x4_f32 a[0:3], v25, v41, a[0:3]
	v_mfma_f32_16x16x4_f32 a[4:7], v25, v57, a[4:7]
	v_cmp_eq_u32_e32 vcc, 0, v71
	s_waitcnt vmcnt(0)
	v_cvt_f32_f16_e32 v60, v60
	v_cvt_f32_f16_e32 v61, v61
	v_cvt_f32_f16_e32 v62, v62
	v_cvt_f32_f16_e32 v63, v63
	v_cvt_f32_f16_e32 v64, v64
	v_cvt_f32_f16_e32 v65, v65
	v_cvt_f32_f16_e32 v66, v66
	v_cvt_f32_f16_e32 v67, v67
	v_add_f32_e32 v60, v58, v60
	v_add_f32_e32 v64, v59, v64
	v_add_f32_e32 v61, v58, v61
	v_add_f32_e32 v65, v59, v65
	v_add_f32_e32 v62, v58, v62
	v_add_f32_e32 v66, v59, v66
	v_add_f32_e32 v63, v58, v63
	v_add_f32_e32 v67, v59, v67
	s_nop 1
	v_accvgpr_read_b32 v2, a0
	v_accvgpr_read_b32 v3, a1
	v_accvgpr_read_b32 v4, a2
	v_accvgpr_read_b32 v5, a3
	v_accvgpr_read_b32 v6, a4
	v_accvgpr_read_b32 v7, a5
	v_accvgpr_read_b32 v8, a6
	v_accvgpr_read_b32 v9, a7
	v_add_f32_e32 v2, v2, v60
	v_add_f32_e32 v3, v3, v61
	v_add_f32_e32 v4, v4, v62
	v_add_f32_e32 v5, v5, v63
	v_add_f32_e32 v6, v6, v64
	v_add_f32_e32 v7, v7, v65
	v_add_f32_e32 v8, v8, v66
	v_add_f32_e32 v9, v9, v67
	v_max_f32_e32 v2, 0, v2
	v_max_f32_e32 v3, 0, v3
	v_max_f32_e32 v4, 0, v4
	v_max_f32_e32 v5, 0, v5
	v_max_f32_e32 v6, 0, v6
	v_max_f32_e32 v7, 0, v7
	v_max_f32_e32 v8, 0, v8
	v_max_f32_e32 v9, 0, v9
	v_mul_f32_e32 v6, v69, v6
	v_mul_f32_e32 v7, v69, v7
	v_mul_f32_e32 v8, v69, v8
	v_mul_f32_e32 v9, v69, v9
	v_fmac_f32_e32 v6, v68, v2
	v_fmac_f32_e32 v7, v68, v3
	v_fmac_f32_e32 v8, v68, v4
	v_fmac_f32_e32 v9, v68, v5
	v_add_f32_dpp v6, v6, v6 quad_perm:[1,0,3,2] row_mask:0xf bank_mask:0xf
	v_add_f32_dpp v7, v7, v7 quad_perm:[1,0,3,2] row_mask:0xf bank_mask:0xf
	v_add_f32_dpp v8, v8, v8 quad_perm:[1,0,3,2] row_mask:0xf bank_mask:0xf
	v_add_f32_dpp v9, v9, v9 quad_perm:[1,0,3,2] row_mask:0xf bank_mask:0xf
	v_add_f32_dpp v6, v6, v6 quad_perm:[2,3,0,1] row_mask:0xf bank_mask:0xf
	v_add_f32_dpp v7, v7, v7 quad_perm:[2,3,0,1] row_mask:0xf bank_mask:0xf
	v_add_f32_dpp v8, v8, v8 quad_perm:[2,3,0,1] row_mask:0xf bank_mask:0xf
	v_add_f32_dpp v9, v9, v9 quad_perm:[2,3,0,1] row_mask:0xf bank_mask:0xf
	v_add_f32_dpp v6, v6, v6 row_half_mirror row_mask:0xf bank_mask:0xf
	v_add_f32_dpp v7, v7, v7 row_half_mirror row_mask:0xf bank_mask:0xf
	v_add_f32_dpp v8, v8, v8 row_half_mirror row_mask:0xf bank_mask:0xf
	v_add_f32_dpp v9, v9, v9 row_half_mirror row_mask:0xf bank_mask:0xf
	v_add_f32_dpp v6, v6, v6 row_mirror row_mask:0xf bank_mask:0xf
	v_add_f32_dpp v7, v7, v7 row_mirror row_mask:0xf bank_mask:0xf
	v_add_f32_dpp v8, v8, v8 row_mirror row_mask:0xf bank_mask:0xf
	v_add_f32_dpp v9, v9, v9 row_mirror row_mask:0xf bank_mask:0xf
	s_and_saveexec_b64 s[2:3], vcc
	ds_write_b128 v76, v[6:9]
	s_or_b64 exec, exec, s[2:3]
	v_cmp_gt_u32_e32 vcc, 16, v0
	s_waitcnt lgkmcnt(0)
	s_barrier
	s_and_saveexec_b64 s[2:3], vcc
	s_cbranch_execz .Lfinal_done
	v_lshlrev_b32_e32 v1, 2, v0
	v_add_u32_e32 v1, 0x1000, v1
	ds_read2_b32 v[2:3], v1 offset0:32 offset1:48
	v_or_b32_e32 v0, s12, v0
	v_ashrrev_i32_e32 v1, 31, v0
	v_lshl_add_u64 v[0:1], v[0:1], 2, s[18:19]
	s_waitcnt lgkmcnt(0)
	v_add_f32_e32 v2, v2, v3
	v_add_f32_e32 v2, s13, v2
	global_store_dword v[0:1], v2, off

	.amdhsa_kernel _Z12final_kernelPKDF16_S0_PKfS2_S2_S2_Pf
		.amdhsa_group_segment_fixed_size 4352
		.amdhsa_private_segment_fixed_size 0
		.amdhsa_kernarg_size 56
		.amdhsa_user_sgpr_count 2
		.amdhsa_user_sgpr_dispatch_ptr 0
		.amdhsa_user_sgpr_queue_ptr 0
		.amdhsa_user_sgpr_kernarg_segment_ptr 1
		.amdhsa_user_sgpr_dispatch_id 0
		.amdhsa_user_sgpr_kernarg_preload_length 0
		.amdhsa_user_sgpr_kernarg_preload_offset 0
		.amdhsa_user_sgpr_private_segment_size 0
		.amdhsa_uses_dynamic_stack 0
		.amdhsa_enable_private_segment 0
		.amdhsa_system_sgpr_workgroup_id_x 1
		.amdhsa_system_sgpr_workgroup_id_y 0
		.amdhsa_system_sgpr_workgroup_id_z 0
		.amdhsa_system_sgpr_workgroup_info 0
		.amdhsa_system_vgpr_workitem_id 0
		.amdhsa_next_free_vgpr 88
		.amdhsa_next_free_sgpr 24
		.amdhsa_accum_offset 80
		.amdhsa_reserve_vcc 1
		.amdhsa_float_round_mode_32 0
		.amdhsa_float_round_mode_16_64 0
		.amdhsa_float_denorm_mode_32 3
		.amdhsa_float_denorm_mode_16_64 3
		.amdhsa_dx10_clamp 1
		.amdhsa_ieee_mode 1
		.amdhsa_fp16_overflow 0
		.amdhsa_tg_split 0
		.amdhsa_exception_fp_ieee_invalid_op 0
		.amdhsa_exception_fp_denorm_src 0
		.amdhsa_exception_fp_ieee_div_zero 0
		.amdhsa_exception_fp_ieee_overflow 0
		.amdhsa_exception_fp_ieee_underflow 0
		.amdhsa_exception_fp_ieee_inexact 0
		.amdhsa_exception_int_div_zero 0
	.end_amdhsa_kernel

amdhsa.kernels:
  - .agpr_count:     8
    .args:
      - .actual_access:  read_only
        .address_space:  global
        .offset:         0
        .size:           8
        .value_kind:     global_buffer
      - .actual_access:  read_only
        .address_space:  global
        .offset:         8
        .size:           8
        .value_kind:     global_buffer
      - .actual_access:  read_only
        .address_space:  global
        .offset:         16
        .size:           8
        .value_kind:     global_buffer
      - .actual_access:  read_only
        .address_space:  global
        .offset:         24
        .size:           8
        .value_kind:     global_buffer
      - .actual_access:  write_only
        .address_space:  global
        .offset:         32
        .size:           8
        .value_kind:     global_buffer
      - .actual_access:  write_only
        .address_space:  global
        .offset:         40
        .size:           8
        .value_kind:     global_buffer
    .group_segment_fixed_size: 4224
    .kernarg_segment_align: 8
    .kernarg_segment_size: 48
    .language:       OpenCL C
    .language_version:
      - 2
      - 0
    .max_flat_workgroup_size: 128
    .name:           _Z11init_kernelPKfS0_S0_S0_PDF16_S1_
    .private_segment_fixed_size: 0
    .sgpr_count:     22
    .sgpr_spill_count: 0
    .symbol:         _Z11init_kernelPKfS0_S0_S0_PDF16_S1_.kd
    .uniform_work_group_size: 1
    .uses_dynamic_stack: false
    .vgpr_count:     52
    .vgpr_spill_count: 0
    .wavefront_size: 64
  - .agpr_count:     8
    .args:
      - .actual_access:  read_only
        .address_space:  global
        .offset:         0
        .size:           8
        .value_kind:     global_buffer
      - .actual_access:  read_only
        .address_space:  global
        .offset:         8
        .size:           8
        .value_kind:     global_buffer
      - .actual_access:  read_only
        .address_space:  global
        .offset:         16
        .size:           8
        .value_kind:     global_buffer
      - .actual_access:  read_only
        .address_space:  global
        .offset:         24
        .size:           8
        .value_kind:     global_buffer
      - .actual_access:  read_only
        .address_space:  global
        .offset:         32
        .size:           8
        .value_kind:     global_buffer
      - .actual_access:  read_only
        .address_space:  global
        .offset:         40
        .size:           8
        .value_kind:     global_buffer
      - .actual_access:  write_only
        .address_space:  global
        .offset:         48
        .size:           8
        .value_kind:     global_buffer
    .group_segment_fixed_size: 4352
    .kernarg_segment_align: 8
    .kernarg_segment_size: 56
    .language:       OpenCL C
    .language_version:
      - 2
      - 0
    .max_flat_workgroup_size: 128
    .name:           _Z12final_kernelPKDF16_S0_PKfS2_S2_S2_Pf
    .private_segment_fixed_size: 0
    .sgpr_count:     30
    .sgpr_spill_count: 0
    .symbol:         _Z12final_kernelPKDF16_S0_PKfS2_S2_S2_Pf.kd
    .uniform_work_group_size: 1
    .uses_dynamic_stack: false
    .vgpr_count:     88
    .vgpr_spill_count: 0
    .wavefront_size: 64
  - .agpr_count:     0
    .args:
      - .actual_access:  read_only
        .address_space:  global
        .offset:         0
        .size:           8
        .value_kind:     global_buffer
      - .actual_access:  read_only
        .address_space:  global
        .offset:         8
        .size:           8
        .value_kind:     global_buffer
      - .actual_access:  read_only
        .address_space:  global
        .offset:         16
        .size:           8
        .value_kind:     global_buffer
      - .actual_access:  read_only
        .address_space:  global
        .offset:         24
        .size:           8
        .value_kind:     global_buffer
      - .actual_access:  read_only
        .address_space:  global
        .offset:         32
        .size:           8
        .value_kind:     global_buffer
      - .actual_access:  read_only
        .address_space:  global
        .offset:         40
        .size:           8
        .value_kind:     global_buffer
      - .actual_access:  read_only
        .address_space:  global
        .offset:         48
        .size:           8
        .value_kind:     global_buffer
      - .actual_access:  read_only
        .address_space:  global
        .offset:         56
        .size:           8
        .value_kind:     global_buffer
      - .actual_access:  read_only
        .address_space:  global
        .offset:         64
        .size:           8
        .value_kind:     global_buffer
      - .actual_access:  read_only
        .address_space:  global
        .offset:         72
        .size:           8
        .value_kind:     global_buffer
      - .address_space:  global
        .offset:         80
        .size:           8
        .value_kind:     global_buffer
    .group_segment_fixed_size: 16896
    .kernarg_segment_align: 8
    .kernarg_segment_size: 88
    .language:       OpenCL C
    .language_version:
      - 2
      - 0
    .max_flat_workgroup_size: 128
    .name:           _Z11edge_kernelILi36ELb1EEvPKfS1_PKDF16_PKiS5_S1_S1_S1_S1_S1_PDF16_
    .private_segment_fixed_size: 0
    .sgpr_count:     45
    .sgpr_spill_count: 0
    .symbol:         _Z11edge_kernelILi36ELb1EEvPKfS1_PKDF16_PKiS5_S1_S1_S1_S1_S1_PDF16_.kd
    .uniform_work_group_size: 1
    .uses_dynamic_stack: false
    .vgpr_count:     168
    .vgpr_spill_count: 0
    .wavefront_size: 64
  - .agpr_count:     0
    .args:
      - .actual_access:  read_only
        .address_space:  global
        .offset:         0
        .size:           8
        .value_kind:     global_buffer
      - .actual_access:  read_only
        .address_space:  global
        .offset:         8
        .size:           8
        .value_kind:     global_buffer
      - .actual_access:  read_only
        .address_space:  global
        .offset:         16
        .size:           8
        .value_kind:     global_buffer
      - .actual_access:  read_only
        .address_space:  global
        .offset:         24
        .size:           8
        .value_kind:     global_buffer
      - .actual_access:  read_only
        .address_space:  global
        .offset:         32
        .size:           8
        .value_kind:     global_buffer
      - .actual_access:  read_only
        .address_space:  global
        .offset:         40
        .size:           8
        .value_kind:     global_buffer
      - .actual_access:  read_only
        .address_space:  global
        .offset:         48
        .size:           8
        .value_kind:     global_buffer
      - .actual_access:  read_only
        .address_space:  global
        .offset:         56
        .size:           8
        .value_kind:     global_buffer
      - .actual_access:  read_only
        .address_space:  global
        .offset:         64
        .size:           8
        .value_kind:     global_buffer
      - .actual_access:  read_only
        .address_space:  global
        .offset:         72
        .size:           8
        .value_kind:     global_buffer
      - .address_space:  global
        .offset:         80
        .size:           8
        .value_kind:     global_buffer
    .group_segment_fixed_size: 16896
    .kernarg_segment_align: 8
    .kernarg_segment_size: 88
    .language:       OpenCL C
    .language_version:
      - 2
      - 0
    .max_flat_workgroup_size: 128
    .name:           _Z11edge_kernelILi64ELb0EEvPKfS1_PKDF16_PKiS5_S1_S1_S1_S1_S1_PDF16_
    .private_segment_fixed_size: 0
    .sgpr_count:     44
    .sgpr_spill_count: 0
    .symbol:         _Z11edge_kernelILi64ELb0EEvPKfS1_PKDF16_PKiS5_S1_S1_S1_S1_S1_PDF16_.kd
    .uniform_work_group_size: 1
    .uses_dynamic_stack: false
    .vgpr_count:     168
    .vgpr_spill_count: 0
    .wavefront_size: 64
